# occ3stag
# speedup vs baseline: 1.0245x; 1.0245x over previous
_Z10gae_kernelPKfPKiS2_S0_S0_S0_PfS3_:
	s_load_dwordx8 s[4:11], s[0:1], 0x0
	s_load_dwordx4 s[12:15], s[0:1], 0x20
	v_and_b32_e32 v64, 63, v0
	v_lshrrev_b32_e32 v1, 6, v0
	s_mov_b32 s3, 0
	s_lshl_b64 s[2:3], s[2:3], 11
	v_lshlrev_b32_e32 v2, 9, v1
	v_lshlrev_b32_e32 v3, 2, v64
	v_or3_b32 v2, s2, v2, v3
	v_mov_b32_e32 v3, s3
	v_lshlrev_b64 v[18:19], 2, v[2:3]
	s_waitcnt lgkmcnt(0)
	v_lshl_add_u64 v[54:55], s[14:15], 0, v[18:19]
	v_lshl_add_u64 v[52:53], s[6:7], 0, v[18:19]
	global_load_dwordx4 v[10:13], v[54:55], off nt
	global_load_dwordx4 v[14:17], v[52:53], off nt
	v_lshl_add_u64 v[56:57], s[8:9], 0, v[18:19]
	global_load_dwordx4 v[20:23], v[56:57], off nt
	v_lshl_add_u64 v[58:59], s[12:13], 0, v[18:19]
	global_load_dwordx4 v[24:27], v[58:59], off nt
	v_lshl_add_u64 v[60:61], s[4:5], 0, v[18:19]
	global_load_dwordx4 v[28:31], v[60:61], off nt
	v_lshl_add_u64 v[62:63], s[10:11], 0, v[18:19]
	global_load_dwordx4 v[2:5], v[62:63], off nt
	s_waitcnt vmcnt(5)
	global_load_dwordx4 v[32:35], v[60:61], off offset:1024 nt
	global_load_dwordx4 v[36:39], v[52:53], off offset:1024 nt
	global_load_dwordx4 v[40:43], v[56:57], off offset:1024 nt
	global_load_dwordx4 v[6:9], v[62:63], off offset:1024 nt
	global_load_dwordx4 v[44:47], v[58:59], off offset:1024 nt
	global_load_dwordx4 v[48:51], v[54:55], off offset:1024 nt
	v_mov_b32_e32 v66, 0
	v_mov_b32_e32 v68, 1.0
	v_mov_b32_e32 v69, 0
	v_mov_b32_e32 v70, 1.0
	v_mov_b32_e32 v71, 0
	v_mov_b32_e32 v72, 1.0
	v_bfe_u32 v73, v0, 4, 2
	v_cmp_gt_u32_e64 s[4:5], 16, v64
	v_mov_b32_e32 v65, 0
	v_mov_b32_e32 v67, 1.0
	s_waitcnt vmcnt(11)
	v_mul_f32_e32 v12, 0x3f7d70a4, v12
	s_waitcnt vmcnt(10)
	v_cmp_eq_u32_e32 vcc, 0, v14
	v_mul_f32_e32 v13, 0x3f7d70a4, v13
	v_mul_f32_e32 v10, 0x3f7d70a4, v10
	v_cndmask_b32_e64 v14, 0, 1.0, vcc
	s_waitcnt vmcnt(9)
	v_cmp_eq_u32_e32 vcc, 0, v20
	v_mul_f32_e32 v11, 0x3f7d70a4, v11
	s_waitcnt vmcnt(8)
	v_mul_f32_e32 v26, v26, v12
	v_cndmask_b32_e64 v20, 0, 1.0, vcc
	v_cmp_eq_u32_e32 vcc, 0, v15
	v_mul_f32_e32 v27, v27, v13
	v_mul_f32_e32 v24, v24, v10
	v_cndmask_b32_e64 v15, 0, 1.0, vcc
	v_cmp_eq_u32_e32 vcc, 0, v21
	v_mul_f32_e32 v25, v25, v11
	v_mul_f32_e32 v12, 0x3f733333, v12
	v_cndmask_b32_e64 v21, 0, 1.0, vcc
	v_cmp_eq_u32_e32 vcc, 0, v16
	v_mul_f32_e32 v13, 0x3f733333, v13
	v_mul_f32_e32 v10, 0x3f733333, v10
	v_cndmask_b32_e64 v16, 0, 1.0, vcc
	v_cmp_eq_u32_e32 vcc, 0, v22
	s_waitcnt vmcnt(7)
	v_fma_f32 v16, v26, v16, v30
	v_mul_f32_e32 v11, 0x3f733333, v11
	v_cndmask_b32_e64 v22, 0, 1.0, vcc
	v_cmp_eq_u32_e32 vcc, 0, v17
	v_fma_f32 v14, v24, v14, v28
	v_fma_f32 v15, v25, v15, v29
	v_cndmask_b32_e64 v17, 0, 1.0, vcc
	v_cmp_eq_u32_e32 vcc, 0, v23
	v_fmac_f32_e32 v31, v27, v17
	v_mul_f32_e32 v22, v12, v22
	v_cndmask_b32_e64 v23, 0, 1.0, vcc
	v_mul_f32_e32 v23, v13, v23
	s_waitcnt vmcnt(6)
	v_sub_f32_e32 v12, v16, v4
	v_sub_f32_e32 v13, v31, v5
	v_mul_f32_e32 v20, v10, v20
	v_mul_f32_e32 v21, v11, v21
	v_sub_f32_e32 v10, v14, v2
	v_sub_f32_e32 v11, v15, v3
	v_mul_f32_e32 v14, v23, v22
	v_fma_f32 v15, v22, v13, v12
	v_mul_f32_e32 v14, v14, v21
	v_fma_f32 v15, v21, v15, v11
	v_mul_f32_e32 v14, v14, v20
	v_fma_f32 v24, v20, v15, v10
	v_mov_b32_e32 v16, 1.0
	v_mov_b32_dpp v68, v14 row_shl:1 row_mask:0xf bank_mask:0xf
	v_mov_b32_dpp v66, v24 row_shl:1 row_mask:0xf bank_mask:0xf
	v_mul_f32_e32 v15, v14, v68
	v_fmac_f32_e32 v24, v14, v66
	v_cmp_eq_u32_e32 vcc, 2, v73
	v_mov_b32_dpp v70, v15 row_shl:2 row_mask:0xf bank_mask:0xf
	v_mov_b32_dpp v69, v24 row_shl:2 row_mask:0xf bank_mask:0xf
	v_mul_f32_e32 v14, v15, v70
	v_fmac_f32_e32 v24, v15, v69
	v_mov_b32_e32 v15, 0
	v_mov_b32_dpp v72, v14 row_shl:4 row_mask:0xf bank_mask:0xf
	v_mov_b32_dpp v71, v24 row_shl:4 row_mask:0xf bank_mask:0xf
	v_fmac_f32_e32 v24, v14, v71
	v_mul_f32_e32 v14, v14, v72
	s_nop 0
	v_mov_b32_dpp v15, v24 row_shl:8 row_mask:0xf bank_mask:0xf
	v_mov_b32_dpp v16, v14 row_shl:8 row_mask:0xf bank_mask:0xf
	v_fmac_f32_e32 v24, v14, v15
	v_mul_f32_e32 v14, v14, v16
	v_readlane_b32 s9, v24, 32
	v_readlane_b32 s2, v14, 48
	v_readlane_b32 s8, v14, 32
	v_readlane_b32 s6, v14, 16
	v_mov_b32_e32 v15, s2
	v_mul_f32_e32 v16, s8, v15
	v_cndmask_b32_e32 v15, 1.0, v15, vcc
	v_cmp_eq_u32_e64 s[2:3], 1, v73
	v_readlane_b32 s10, v24, 48
	v_mul_f32_e32 v17, s6, v16
	v_cndmask_b32_e64 v15, v15, v16, s[2:3]
	v_readlane_b32 s7, v24, 16
	v_cndmask_b32_e64 v15, v15, v17, s[4:5]
	v_mov_b32_e32 v16, s9
	v_mov_b32_e32 v17, s10
	v_fmac_f32_e32 v16, s8, v17
	v_mov_b32_e32 v25, s7
	v_cndmask_b32_e32 v17, 0, v17, vcc
	v_fmac_f32_e32 v25, s6, v16
	v_cndmask_b32_e64 v16, v17, v16, s[2:3]
	v_cndmask_b32_e64 v16, v16, v25, s[4:5]
	s_waitcnt vmcnt(4)
	v_cmp_eq_u32_e64 s[6:7], 0, v36
	v_fmac_f32_e32 v24, v14, v16
	v_mul_f32_e32 v28, v14, v15
	s_waitcnt vmcnt(0)
	v_mul_f32_e32 v15, 0x3f7d70a4, v48
	v_cndmask_b32_e64 v14, 0, 1.0, s[6:7]
	v_cmp_eq_u32_e64 s[6:7], 0, v40
	v_mul_f32_e32 v17, v44, v15
	v_mul_f32_e32 v15, 0x3f733333, v15
	v_cndmask_b32_e64 v16, 0, 1.0, s[6:7]
	v_cmp_eq_u32_e64 s[6:7], 0, v37
	v_mul_f32_e32 v25, v15, v16
	v_mul_f32_e32 v16, 0x3f7d70a4, v49
	v_cndmask_b32_e64 v15, 0, 1.0, s[6:7]
	v_cmp_eq_u32_e64 s[6:7], 0, v41
	v_fma_f32 v14, v17, v14, v32
	v_mul_f32_e32 v26, v45, v16
	v_cndmask_b32_e64 v17, 0, 1.0, s[6:7]
	v_mul_f32_e32 v16, 0x3f733333, v16
	v_fma_f32 v15, v26, v15, v33
	v_mul_f32_e32 v26, v16, v17
	v_mul_f32_e32 v17, 0x3f7d70a4, v50
	v_cmp_eq_u32_e64 s[6:7], 0, v38
	v_mul_f32_e32 v29, v46, v17
	v_mul_f32_e32 v17, 0x3f733333, v17
	v_cndmask_b32_e64 v16, 0, 1.0, s[6:7]
	v_cmp_eq_u32_e64 s[6:7], 0, v42
	v_fma_f32 v16, v29, v16, v34
	v_mul_f32_e32 v29, 0x3f7d70a4, v51
	v_cndmask_b32_e64 v27, 0, 1.0, s[6:7]
	v_cmp_eq_u32_e64 s[6:7], 0, v39
	v_mul_f32_e32 v27, v17, v27
	v_mul_f32_e32 v31, v47, v29
	v_cndmask_b32_e64 v17, 0, 1.0, s[6:7]
	v_cmp_eq_u32_e64 s[6:7], 0, v43
	v_fmac_f32_e32 v35, v31, v17
	v_mul_f32_e32 v29, 0x3f733333, v29
	v_cndmask_b32_e64 v30, 0, 1.0, s[6:7]
	v_sub_f32_e32 v16, v16, v8
	v_sub_f32_e32 v17, v35, v9
	v_mul_f32_e32 v29, v29, v30
	v_sub_f32_e32 v15, v15, v7
	v_fma_f32 v30, v27, v17, v16
	v_mul_f32_e32 v31, v29, v27
	v_sub_f32_e32 v14, v14, v6
	v_fma_f32 v30, v26, v30, v15
	v_mul_f32_e32 v31, v31, v26
	v_fma_f32 v30, v25, v30, v14
	v_mul_f32_e32 v31, v31, v25
	v_mov_b32_e32 v32, 0
	v_mov_b32_e32 v33, 1.0
	s_nop 0
	v_mov_b32_dpp v32, v30 row_shl:1 row_mask:0xf bank_mask:0xf
	v_mov_b32_dpp v33, v31 row_shl:1 row_mask:0xf bank_mask:0xf
	v_fmac_f32_e32 v30, v31, v32
	v_mul_f32_e32 v31, v31, v33
	v_mov_b32_e32 v32, 0
	v_mov_b32_e32 v33, 1.0
	s_nop 0
	v_mov_b32_dpp v32, v30 row_shl:2 row_mask:0xf bank_mask:0xf
	v_mov_b32_dpp v33, v31 row_shl:2 row_mask:0xf bank_mask:0xf
	v_fmac_f32_e32 v30, v31, v32
	v_mul_f32_e32 v31, v31, v33
	v_mov_b32_e32 v32, 0
	v_mov_b32_e32 v33, 1.0
	s_nop 0
	v_mov_b32_dpp v32, v30 row_shl:4 row_mask:0xf bank_mask:0xf
	v_mov_b32_dpp v33, v31 row_shl:4 row_mask:0xf bank_mask:0xf
	v_fmac_f32_e32 v30, v31, v32
	v_mul_f32_e32 v31, v31, v33
	s_nop 0
	v_mov_b32_dpp v65, v30 row_shl:8 row_mask:0xf bank_mask:0xf
	v_mov_b32_dpp v67, v31 row_shl:8 row_mask:0xf bank_mask:0xf
	v_fmac_f32_e32 v30, v31, v65
	v_mul_f32_e32 v31, v31, v67
	v_readlane_b32 s9, v30, 32
	v_readlane_b32 s10, v31, 48
	v_readlane_b32 s8, v31, 32
	v_readlane_b32 s6, v31, 16
	v_mov_b32_e32 v32, s10
	v_mul_f32_e32 v33, s8, v32
	v_cndmask_b32_e32 v32, 1.0, v32, vcc
	v_readlane_b32 s11, v30, 48
	v_mul_f32_e32 v34, s6, v33
	v_cndmask_b32_e64 v32, v32, v33, s[2:3]
	v_readlane_b32 s7, v30, 16
	v_cndmask_b32_e64 v32, v32, v34, s[4:5]
	v_mov_b32_e32 v33, s9
	v_mov_b32_e32 v34, s11
	v_fmac_f32_e32 v33, s8, v34
	v_mov_b32_e32 v35, s7
	v_cndmask_b32_e32 v34, 0, v34, vcc
	v_fmac_f32_e32 v35, s6, v33
	v_cndmask_b32_e64 v33, v34, v33, s[2:3]
	v_cndmask_b32_e64 v33, v33, v35, s[4:5]
	v_fmac_f32_e32 v30, v31, v33
	v_mul_f32_e32 v31, v31, v32
	v_readlane_b32 s6, v28, 0
	v_readlane_b32 s7, v24, 0
	v_readlane_b32 s4, v31, 0
	v_readlane_b32 s5, v30, 0
	v_cmp_eq_u32_e32 vcc, 0, v64
	s_and_saveexec_b64 s[2:3], vcc
	s_cbranch_execz .LBB0_4
	v_mov_b32_e32 v32, s4
	v_mov_b32_e32 v33, s7
	v_mov_b32_e32 v34, s5
	v_mul_f32_e32 v32, s6, v32
	v_lshlrev_b32_e32 v1, 2, v1
	v_fmac_f32_e32 v33, s6, v34
	ds_write2_b32 v1, v32, v33 offset1:4
